# baseline (speedup 1.0000x reference)
.LBB0_17:
	v_mfma_f32_32x32x16_bf16 v[112:127], a[192:195], a[128:131], v[0:15]
	v_exp_f32_e32 v48, v48
	v_exp_f32_e32 v49, v49
	ds_read_b64_tr_b16 v[172:173], v215 offset:0
	v_cvt_pk_bf16_f32 v164, v128, v129
	v_exp_f32_e32 v50, v50
	v_exp_f32_e32 v51, v51
	v_mfma_f32_32x32x16_bf16 v[96:111], a[192:195], a[160:163], v[16:31]
	ds_read_b64_tr_b16 v[174:175], v215 offset:0x800
	v_cvt_pk_bf16_f32 v165, v130, v131
	v_mfma_f32_32x32x16_bf16 v[80:95], a[224:227], a[128:131], v[0:15]
	ds_read_b64_tr_b16 v[184:185], v215 offset:0x200
	v_exp_f32_e32 v239, v52
	v_exp_f32_e32 v240, v53
	v_cvt_pk_bf16_f32 v166, v132, v133
	v_mfma_f32_32x32x16_bf16 v[64:79], a[224:227], a[160:163], v[16:31]
	ds_read_b64_tr_b16 v[186:187], v215 offset:0xa00
	ds_read_b64_tr_b16 v[180:181], v215 offset:0x400
	v_exp_f32_e32 v241, v54
	v_exp_f32_e32 v242, v55
	v_cvt_pk_bf16_f32 v167, v134, v135
	v_exp_f32_e32 v227, v56
	v_exp_f32_e32 v228, v57
	v_mfma_f32_32x32x16_bf16 v[112:127], a[196:199], a[132:135], v[112:127]
	ds_read_b64_tr_b16 v[182:183], v215 offset:0xc00
	v_cvt_pk_bf16_f32 v128, v136, v137
	v_exp_f32_e32 v229, v58
	v_exp_f32_e32 v230, v59
	v_mfma_f32_32x32x16_bf16 v[96:111], a[196:199], a[164:167], v[96:111]
	ds_read_b64_tr_b16 v[188:189], v215 offset:0x600
	v_cvt_pk_bf16_f32 v129, v138, v139
	v_exp_f32_e32 v231, v60
	v_exp_f32_e32 v232, v61
	v_mfma_f32_32x32x16_bf16 v[80:95], a[228:231], a[132:135], v[80:95]
	ds_read_b64_tr_b16 v[190:191], v215 offset:0xe00
	v_cvt_pk_bf16_f32 v130, v140, v141
	v_mfma_f32_32x32x16_bf16 v[64:79], a[228:231], a[164:167], v[64:79]
	ds_read_b64_tr_b16 v[176:177], v215 offset:0x1000
	v_exp_f32_e32 v233, v62
	v_exp_f32_e32 v234, v63
	ds_read_b64_tr_b16 v[178:179], v215 offset:0x1800
	v_cvt_pk_bf16_f32 v131, v142, v143
	v_exp_f32_e32 v141, v32
	v_exp_f32_e32 v142, v33
	v_mfma_f32_32x32x16_bf16 v[112:127], a[200:203], a[136:139], v[112:127]
	ds_read_b64_tr_b16 v[168:169], v215 offset:0x1200
	v_cvt_pk_bf16_f32 v192, v144, v145
	v_exp_f32_e32 v143, v34
	v_mfma_f32_32x32x16_bf16 v[96:111], a[200:203], a[168:171], v[96:111]
	ds_read_b64_tr_b16 v[170:171], v215 offset:0x1a00
	v_exp_f32_e32 v243, v35
	v_cvt_pk_bf16_f32 v193, v146, v147
	v_mfma_f32_32x32x16_bf16 v[80:95], a[232:235], a[136:139], v[80:95]
	ds_read_b64_tr_b16 v[160:161], v215 offset:0x1400
	v_exp_f32_e32 v244, v36
	v_exp_f32_e32 v245, v37
	v_cvt_pk_bf16_f32 v194, v148, v149
	v_mfma_f32_32x32x16_bf16 v[64:79], a[232:235], a[168:171], v[64:79]
	ds_read_b64_tr_b16 v[162:163], v215 offset:0x1c00
	ds_read_b64_tr_b16 v[136:137], v215 offset:0x1600
	v_exp_f32_e32 v246, v38
	v_exp_f32_e32 v247, v39
	v_cvt_pk_bf16_f32 v195, v150, v151
	v_exp_f32_e32 v148, v40
	v_exp_f32_e32 v149, v41
	v_mfma_f32_32x32x16_bf16 v[112:127], a[204:207], a[140:143], v[112:127]
	ds_read_b64_tr_b16 v[138:139], v215 offset:0x1e00
	v_cvt_pk_bf16_f32 v144, v152, v153
	v_exp_f32_e32 v150, v42
	v_exp_f32_e32 v151, v43
	v_mfma_f32_32x32x16_bf16 v[96:111], a[204:207], a[172:175], v[96:111]
	ds_read_b64_tr_b16 v[132:133], v215 offset:0x2000
	v_cvt_pk_bf16_f32 v145, v154, v155
	v_exp_f32_e32 v152, v44
	v_exp_f32_e32 v153, v45
	v_mfma_f32_32x32x16_bf16 v[80:95], a[236:239], a[140:143], v[80:95]
	ds_read_b64_tr_b16 v[134:135], v215 offset:0x2800
	v_cvt_pk_bf16_f32 v146, v156, v157
	v_mfma_f32_32x32x16_bf16 v[64:79], a[236:239], a[172:175], v[64:79]
	ds_read_b64_tr_b16 v[60:61], v215 offset:0x2200
	v_exp_f32_e32 v154, v46
	v_exp_f32_e32 v155, v47
	ds_read_b64_tr_b16 v[62:63], v215 offset:0x2a00
	v_cvt_pk_bf16_f32 v147, v158, v159
	s_mov_b32 s0, s29
	v_mfma_f32_32x32x16_bf16 v[112:127], a[208:211], a[144:147], v[112:127]
	ds_read_b64_tr_b16 v[56:57], v215 offset:0x2400
	v_cvt_pk_bf16_f32 v52, v48, v49
	v_add_f32_e32 v32, v236, v48
	v_add_f32_e32 v33, v235, v49
	s_add_i32 s57, s58, s59
	s_and_b32 s57, s57, 0x7ffff
	s_mov_b32 s33, s57
	s_mov_b32 s1, s33
	v_mfma_f32_32x32x16_bf16 v[96:111], a[208:211], a[176:179], v[96:111]
	ds_read_b64_tr_b16 v[58:59], v215 offset:0x2c00
	v_cvt_pk_bf16_f32 v53, v50, v51
	v_add_f32_e32 v32, v32, v50
	v_add_f32_e32 v33, v33, v51
	s_mov_b32 s35, s20
	v_mfma_f32_32x32x16_bf16 v[80:95], a[240:243], a[144:147], v[80:95]
	ds_read_b64_tr_b16 v[48:49], v215 offset:0x2600
	v_cvt_pk_bf16_f32 v54, v239, v240
	v_add_f32_e32 v32, v32, v239
	v_add_f32_e32 v33, v33, v240
	s_add_i32 s36, s57, 0x400
	v_mfma_f32_32x32x16_bf16 v[64:79], a[240:243], a[176:179], v[64:79]
	ds_read_b64_tr_b16 v[50:51], v215 offset:0x2e00
	ds_read_b64_tr_b16 v[44:45], v215 offset:0x3000
	v_cvt_pk_bf16_f32 v55, v241, v242
	v_add_f32_e32 v32, v32, v241
	v_add_f32_e32 v33, v33, v242
	s_mov_b32 s37, s21
	v_mfma_f32_32x32x16_bf16 v[112:127], a[212:215], a[148:151], v[112:127]
	ds_read_b64_tr_b16 v[46:47], v215 offset:0x3800
	v_add_f32_e32 v32, v32, v227
	v_add_f32_e32 v33, v33, v228
	s_add_i32 s34, s57, 0x800
	s_mov_b32 s38, s34
	v_mfma_f32_32x32x16_bf16 v[96:111], a[212:215], a[180:183], v[96:111]
	ds_read_b64_tr_b16 v[40:41], v215 offset:0x3200
	v_add_f32_e32 v32, v32, v229
	v_add_f32_e32 v33, v33, v230
	s_mov_b32 s39, s22
	v_mfma_f32_32x32x16_bf16 v[80:95], a[244:247], a[148:151], v[80:95]
	ds_read_b64_tr_b16 v[42:43], v215 offset:0x3a00
	v_add_f32_e32 v32, v32, v231
	v_add_f32_e32 v33, v33, v232
	s_add_i32 s40, s57, 0xc00
	v_mfma_f32_32x32x16_bf16 v[64:79], a[244:247], a[180:183], v[64:79]
	ds_read_b64_tr_b16 v[36:37], v215 offset:0x3400
	ds_read_b64_tr_b16 v[38:39], v215 offset:0x3c00
	v_add_f32_e32 v156, v32, v233
	v_add_f32_e32 v157, v33, v234
	s_mov_b32 s41, s23
	v_mfma_f32_32x32x16_bf16 v[112:127], a[216:219], a[152:155], v[112:127]
	ds_read_b64_tr_b16 v[32:33], v215 offset:0x3600
	v_cvt_pk_bf16_f32 v140, v141, v142
	v_add_f32_e32 v158, v237, v141
	v_add_f32_e32 v142, v238, v142
	s_mov_b32 s42, s58
	v_mfma_f32_32x32x16_bf16 v[96:111], a[216:219], a[184:187], v[96:111]
	ds_read_b64_tr_b16 v[34:35], v215 offset:0x3e00
	v_cvt_pk_bf16_f32 v141, v143, v243
	v_add_f32_e32 v143, v158, v143
	v_add_f32_e32 v158, v142, v243
	v_mfma_f32_32x32x16_bf16 v[80:95], a[248:251], a[152:155], v[80:95]
	s_mov_b32 s43, s24
	v_cvt_pk_bf16_f32 v142, v244, v245
	v_add_f32_e32 v159, v143, v244
	v_add_f32_e32 v158, v158, v245
	v_mfma_f32_32x32x16_bf16 v[64:79], a[248:251], a[184:187], v[64:79]
	s_add_i32 s44, s58, 0x80
	v_cvt_pk_bf16_f32 v143, v246, v247
	v_add_f32_e32 v159, v159, v246
	v_add_f32_e32 v158, v158, v247
	v_mfma_f32_32x32x16_bf16 v[112:127], a[220:223], a[156:159], v[112:127]
	s_mov_b32 s45, s25
	v_add_f32_e32 v159, v159, v148
	v_add_f32_e32 v158, v158, v149
	v_mfma_f32_32x32x16_bf16 v[96:111], a[220:223], a[188:191], v[96:111]
	s_add_i32 s46, s58, 0x800
	v_add_f32_e32 v159, v159, v150
	v_add_f32_e32 v158, v158, v151
	v_mfma_f32_32x32x16_bf16 v[80:95], a[252:255], a[156:159], v[80:95]
	s_mov_b32 s47, s26
	v_add_f32_e32 v159, v159, v152
	v_add_f32_e32 v158, v158, v153
	v_mfma_f32_32x32x16_bf16 v[64:79], a[252:255], a[188:191], v[64:79]
	s_add_i32 s48, s58, 0x880
	v_add_f32_e32 v159, v159, v154
	v_add_f32_e32 v158, v158, v155
	v_add_f32_e32 v156, v156, v157
	s_waitcnt vmcnt(0) lgkmcnt(0)
	s_barrier
	s_mov_b32 m0, s0
	v_mfma_f32_32x32x16_bf16 a[0:15], v[172:175], v[164:167], a[0:15]
	buffer_load_dwordx4 v222, s[12:15], s1 offen lds
	v_mfma_f32_32x32x16_bf16 a[16:31], v[172:175], v[192:195], a[16:31]
	ds_read_b128 a[192:195], v217 offset:0
	s_mov_b32 m0, s35
	v_mfma_f32_32x32x16_bf16 a[32:47], v[184:187], v[164:167], a[32:47]
	buffer_load_dwordx4 v223, s[12:15], s36 offen lds
	v_add_f32_e32 v225, v225, v156
	v_add_f32_e32 v156, v159, v158
	ds_read_b128 a[196:199], v199 offset:0
	v_mfma_f32_32x32x16_bf16 a[48:63], v[184:187], v[192:195], a[48:63]
	ds_read_b128 a[200:203], v198 offset:0
	s_mov_b32 m0, s37
	v_mfma_f32_32x32x16_bf16 a[64:79], v[180:183], v[164:167], a[64:79]
	buffer_load_dwordx4 v222, s[12:15], s38 offen lds
	v_add_f32_e32 v226, v226, v156
	ds_read_b128 a[204:207], v197 offset:0
	v_mfma_f32_32x32x16_bf16 a[80:95], v[180:183], v[192:195], a[80:95]
	ds_read_b128 a[208:211], v217 offset:128
	s_mov_b32 m0, s39
	v_mfma_f32_32x32x16_bf16 a[96:111], v[188:191], v[164:167], a[96:111]
	buffer_load_dwordx4 v223, s[12:15], s40 offen lds
	ds_read_b128 a[212:215], v199 offset:128
	v_mfma_f32_32x32x16_bf16 a[112:127], v[188:191], v[192:195], a[112:127]
	ds_read_b128 a[216:219], v198 offset:128
	s_nop 0
	s_mov_b32 m0, s41
	v_mfma_f32_32x32x16_bf16 a[0:15], v[176:179], v[128:131], a[0:15]
	buffer_load_dwordx4 v196, s[4:7], s42 offen lds
	ds_read_b128 a[220:223], v197 offset:128
	s_cmp_gt_u32 s27, 12
	s_cbranch_scc1 .Lka_done
	s_cmp_gt_u32 s27, 4
	s_cbranch_scc1 .Lka_single
	v_cvt_pk_bf16_f32 v248, v248, v249
	v_cvt_pk_bf16_f32 v249, v250, v251
	v_cvt_pk_bf16_f32 v250, v252, v253
	v_cvt_pk_bf16_f32 v251, v254, v255
	v_lshrrev_b32_e32 v252, 1, v208
	buffer_store_dwordx4 v[248:251], v252, s[12:15], s56 offen sc1
	v_mbcnt_lo_u32_b32 v253, -1, 0
	v_mbcnt_hi_u32_b32 v253, -1, v253
	v_lshlrev_b32_e32 v253, 4, v253
	v_add_u32_e32 v253, s84, v253
	ds_read_b128 v[248:251], v253
	ds_read_b128 v[252:255], v253 offset:1024
	s_cmp_eq_u32 s27, 2
	s_cbranch_scc0 .Lka_nopub
	s_cmp_eq_u32 s50, 0
	s_cbranch_scc0 .Lf1_pub_done
	v_mov_b32_e32 v210, s70
	s_mov_b64 exec, 1
	global_store_dword v209, v210, s[72:73] offset:3072 sc1
	s_mov_b64 exec, -1

.Lka_done:
	v_max3_f32 v156, v112, v113, v80
	v_max3_f32 v157, v114, v115, v81
	s_nop 0
	v_max3_f32 v156, v156, v82, v83
	v_mfma_f32_32x32x16_bf16 a[16:31], v[176:179], v[144:147], a[16:31]
	ds_read_b128 a[224:227], v217 offset:8192
	v_max3_f32 v156, v156, v116, v117
	v_max3_f32 v157, v157, v118, v119
	v_max3_f32 v156, v156, v84, v85
	v_max3_f32 v157, v157, v86, v87
	s_mov_b32 m0, s43
	v_mfma_f32_32x32x16_bf16 a[32:47], v[168:171], v[128:131], a[32:47]
	buffer_load_dwordx4 v196, s[4:7], s44 offen lds
	ds_read_b128 a[228:231], v199 offset:8192
	v_max3_f32 v156, v156, v120, v121
	v_max3_f32 v157, v157, v122, v123
	v_max3_f32 v156, v156, v88, v89
	v_max3_f32 v157, v157, v90, v91
	v_mfma_f32_32x32x16_bf16 a[48:63], v[168:171], v[144:147], a[48:63]
	ds_read_b128 a[232:235], v198 offset:8192
	v_max3_f32 v156, v156, v124, v125
	v_max3_f32 v157, v157, v126, v127
	v_max3_f32 v156, v156, v92, v93
	v_max3_f32 v157, v157, v94, v95
	s_mov_b32 m0, s45
	v_mfma_f32_32x32x16_bf16 a[64:79], v[160:163], v[128:131], a[64:79]
	buffer_load_dwordx4 v196, s[4:7], s46 offen lds
	ds_read_b128 a[236:239], v197 offset:8192
	v_max3_f32 v158, v96, v97, v64
	v_max3_f32 v159, v98, v99, v65
	v_max3_f32 v158, v158, v66, v67
	v_mfma_f32_32x32x16_bf16 a[80:95], v[160:163], v[144:147], a[80:95]
	ds_read_b128 a[240:243], v217 offset:8320
	v_max3_f32 v158, v158, v100, v101
	v_max3_f32 v159, v159, v102, v103
	v_max3_f32 v158, v158, v68, v69
	v_max3_f32 v159, v159, v70, v71
	s_mov_b32 m0, s47
	v_mfma_f32_32x32x16_bf16 a[96:111], v[136:139], v[128:131], a[96:111]
	buffer_load_dwordx4 v196, s[4:7], s48 offen lds
	ds_read_b128 a[244:247], v199 offset:8320
	v_max3_f32 v128, v158, v104, v105
	v_max3_f32 v129, v159, v106, v107
	v_max3_f32 v128, v128, v72, v73
	v_max3_f32 v129, v129, v74, v75
	v_mfma_f32_32x32x16_bf16 a[112:127], v[136:139], v[144:147], a[112:127]
	ds_read_b128 a[248:251], v198 offset:8320
	v_max3_f32 v128, v128, v108, v109
	v_max3_f32 v129, v129, v110, v111
	v_max3_f32 v128, v128, v76, v77
	v_max3_f32 v130, v129, v78, v79
	v_mfma_f32_32x32x16_bf16 a[0:15], v[132:135], v[52:55], a[0:15]
	ds_read_b128 a[252:255], v197 offset:8320
	s_cmp_gt_u32 s27, 4
	s_cbranch_scc1 .Lkb2_done
	s_waitcnt lgkmcnt(8)
	v_pk_add_f32 v[200:201], v[248:249], v[200:201]
	v_pk_add_f32 v[202:203], v[250:251], v[202:203]
	v_pk_add_f32 v[204:205], v[252:253], v[204:205]
	v_pk_add_f32 v[206:207], v[254:255], v[206:207]
	v_cvt_pk_bf16_f32 v248, v248, v249
	v_cvt_pk_bf16_f32 v249, v250, v251
	v_cvt_pk_bf16_f32 v250, v252, v253
	v_cvt_pk_bf16_f32 v251, v254, v255
	v_lshrrev_b32_e32 v252, 1, v208
	buffer_store_dwordx4 v[248:251], v252, s[4:7], s56 offen sc1
	s_add_i32 s56, s56, 0x1000
	s_nop 1
	global_load_dwordx4 v[248:251], v208, s[54:55] nt
	global_load_dwordx4 v[252:255], v208, s[54:55] offset:16 nt
	s_add_u32 s54, s54, 0x2000
	s_addc_u32 s55, s55, 0
	s_mov_b32 m0, s84
	s_nop 0
	buffer_load_dwordx4 v208, s[80:83], s86 offen lds
	s_mov_b32 m0, s85
	s_nop 0
	buffer_load_dwordx4 v208, s[80:83], s86 offen offset:16 lds
	s_add_i32 s86, s86, 0x2000

.LBB0_19:
	s_waitcnt lgkmcnt(0)
	v_mfma_f32_32x32x16_bf16 v[112:127], a[192:195], a[128:131], v[0:15]
	v_exp_f32_e32 v80, v80
	v_exp_f32_e32 v81, v81
	ds_read_b64_tr_b16 v[180:181], v212 offset:0
	v_cvt_pk_bf16_f32 v168, v128, v129
	v_exp_f32_e32 v82, v82
	v_exp_f32_e32 v83, v83
	v_mfma_f32_32x32x16_bf16 v[96:111], a[192:195], a[160:163], v[16:31]
	ds_read_b64_tr_b16 v[182:183], v212 offset:0x800
	v_cvt_pk_bf16_f32 v169, v130, v131
	v_mfma_f32_32x32x16_bf16 v[48:63], a[224:227], a[128:131], v[0:15]
	ds_read_b64_tr_b16 v[184:185], v212 offset:0x200
	v_exp_f32_e32 v239, v84
	v_exp_f32_e32 v240, v85
	v_cvt_pk_bf16_f32 v170, v132, v133
	v_mfma_f32_32x32x16_bf16 v[32:47], a[224:227], a[160:163], v[16:31]
	ds_read_b64_tr_b16 v[186:187], v212 offset:0xa00
	ds_read_b64_tr_b16 v[176:177], v212 offset:0x400
	v_exp_f32_e32 v241, v86
	v_exp_f32_e32 v242, v87
	v_cvt_pk_bf16_f32 v171, v134, v135
	v_exp_f32_e32 v227, v88
	v_exp_f32_e32 v228, v89
	v_mfma_f32_32x32x16_bf16 v[112:127], a[196:199], a[132:135], v[112:127]
	ds_read_b64_tr_b16 v[178:179], v212 offset:0xc00
	v_cvt_pk_bf16_f32 v128, v136, v137
	v_exp_f32_e32 v229, v90
	v_exp_f32_e32 v230, v91
	v_mfma_f32_32x32x16_bf16 v[96:111], a[196:199], a[164:167], v[96:111]
	ds_read_b64_tr_b16 v[188:189], v212 offset:0x600
	v_cvt_pk_bf16_f32 v129, v138, v139
	v_exp_f32_e32 v231, v92
	v_exp_f32_e32 v232, v93
	v_mfma_f32_32x32x16_bf16 v[48:63], a[228:231], a[132:135], v[48:63]
	ds_read_b64_tr_b16 v[190:191], v212 offset:0xe00
	v_cvt_pk_bf16_f32 v130, v140, v141
	v_mfma_f32_32x32x16_bf16 v[32:47], a[228:231], a[164:167], v[32:47]
	ds_read_b64_tr_b16 v[172:173], v212 offset:0x1000
	v_exp_f32_e32 v233, v94
	v_exp_f32_e32 v234, v95
	ds_read_b64_tr_b16 v[174:175], v212 offset:0x1800
	v_cvt_pk_bf16_f32 v131, v142, v143
	v_exp_f32_e32 v141, v64
	v_exp_f32_e32 v142, v65
	v_mfma_f32_32x32x16_bf16 v[112:127], a[200:203], a[136:139], v[112:127]
	ds_read_b64_tr_b16 v[164:165], v212 offset:0x1200
	v_cvt_pk_bf16_f32 v192, v144, v145
	v_exp_f32_e32 v143, v66
	v_mfma_f32_32x32x16_bf16 v[96:111], a[200:203], a[168:171], v[96:111]
	ds_read_b64_tr_b16 v[166:167], v212 offset:0x1a00
	v_exp_f32_e32 v243, v67
	v_cvt_pk_bf16_f32 v193, v146, v147
	v_mfma_f32_32x32x16_bf16 v[48:63], a[232:235], a[136:139], v[48:63]
	ds_read_b64_tr_b16 v[160:161], v212 offset:0x1400
	v_exp_f32_e32 v244, v68
	v_exp_f32_e32 v245, v69
	v_cvt_pk_bf16_f32 v194, v148, v149
	v_mfma_f32_32x32x16_bf16 v[32:47], a[232:235], a[168:171], v[32:47]
	ds_read_b64_tr_b16 v[162:163], v212 offset:0x1c00
	ds_read_b64_tr_b16 v[136:137], v212 offset:0x1600
	v_exp_f32_e32 v246, v70
	v_exp_f32_e32 v247, v71
	v_cvt_pk_bf16_f32 v195, v150, v151
	v_exp_f32_e32 v148, v72
	v_exp_f32_e32 v149, v73
	v_mfma_f32_32x32x16_bf16 v[112:127], a[204:207], a[140:143], v[112:127]
	ds_read_b64_tr_b16 v[138:139], v212 offset:0x1e00
	v_cvt_pk_bf16_f32 v144, v152, v153
	v_exp_f32_e32 v150, v74
	v_exp_f32_e32 v151, v75
	v_mfma_f32_32x32x16_bf16 v[96:111], a[204:207], a[172:175], v[96:111]
	ds_read_b64_tr_b16 v[132:133], v212 offset:0x2000
	v_cvt_pk_bf16_f32 v145, v154, v155
	v_exp_f32_e32 v152, v76
	v_exp_f32_e32 v153, v77
	v_mfma_f32_32x32x16_bf16 v[48:63], a[236:239], a[140:143], v[48:63]
	ds_read_b64_tr_b16 v[134:135], v212 offset:0x2800
	v_cvt_pk_bf16_f32 v146, v156, v157
	v_mfma_f32_32x32x16_bf16 v[32:47], a[236:239], a[172:175], v[32:47]
	ds_read_b64_tr_b16 v[92:93], v212 offset:0x2200
	v_exp_f32_e32 v154, v78
	v_exp_f32_e32 v155, v79
	ds_read_b64_tr_b16 v[94:95], v212 offset:0x2a00
	v_cvt_pk_bf16_f32 v147, v158, v159
	s_mov_b32 s0, s3
	v_mfma_f32_32x32x16_bf16 v[112:127], a[208:211], a[144:147], v[112:127]
	ds_read_b64_tr_b16 v[88:89], v212 offset:0x2400
	v_cvt_pk_bf16_f32 v84, v80, v81
	v_add_f32_e32 v64, v236, v80
	v_add_f32_e32 v65, v235, v81
	s_add_i32 s58, s57, s60
	s_and_b32 s58, s58, 0x7ffff
	s_mov_b32 s1, s58
	v_mfma_f32_32x32x16_bf16 v[96:111], a[208:211], a[176:179], v[96:111]
	ds_read_b64_tr_b16 v[90:91], v212 offset:0x2c00
	v_cvt_pk_bf16_f32 v85, v82, v83
	v_add_f32_e32 v64, v64, v82
	v_add_f32_e32 v65, v65, v83
	s_mov_b32 s35, s10
	v_mfma_f32_32x32x16_bf16 v[48:63], a[240:243], a[144:147], v[48:63]
	ds_read_b64_tr_b16 v[80:81], v212 offset:0x2600
	v_cvt_pk_bf16_f32 v86, v239, v240
	v_add_f32_e32 v64, v64, v239
	v_add_f32_e32 v65, v65, v240
	s_add_i32 s36, s58, 0x400
	v_mfma_f32_32x32x16_bf16 v[32:47], a[240:243], a[176:179], v[32:47]
	ds_read_b64_tr_b16 v[82:83], v212 offset:0x2e00
	ds_read_b64_tr_b16 v[76:77], v212 offset:0x3000
	v_cvt_pk_bf16_f32 v87, v241, v242
	v_add_f32_e32 v64, v64, v241
	v_add_f32_e32 v65, v65, v242
	s_mov_b32 s37, s11
	v_mfma_f32_32x32x16_bf16 v[112:127], a[212:215], a[148:151], v[112:127]
	ds_read_b64_tr_b16 v[78:79], v212 offset:0x3800
	v_add_f32_e32 v64, v64, v227
	v_add_f32_e32 v65, v65, v228
	s_add_i32 s38, s58, 0x800
	v_mfma_f32_32x32x16_bf16 v[96:111], a[212:215], a[180:183], v[96:111]
	ds_read_b64_tr_b16 v[72:73], v212 offset:0x3200
	v_add_f32_e32 v64, v64, v229
	v_add_f32_e32 v65, v65, v230
	s_mov_b32 s39, s16
	v_mfma_f32_32x32x16_bf16 v[48:63], a[244:247], a[148:151], v[48:63]
	ds_read_b64_tr_b16 v[74:75], v212 offset:0x3a00
	v_add_f32_e32 v64, v64, v231
	v_add_f32_e32 v65, v65, v232
	s_add_i32 s40, s58, 0xc00
	v_mfma_f32_32x32x16_bf16 v[32:47], a[244:247], a[180:183], v[32:47]
	ds_read_b64_tr_b16 v[68:69], v212 offset:0x3400
	ds_read_b64_tr_b16 v[70:71], v212 offset:0x3c00
	v_add_f32_e32 v156, v64, v233
	v_add_f32_e32 v157, v65, v234
	s_mov_b32 s41, s2
	v_mfma_f32_32x32x16_bf16 v[112:127], a[216:219], a[152:155], v[112:127]
	ds_read_b64_tr_b16 v[64:65], v212 offset:0x3600
	v_cvt_pk_bf16_f32 v140, v141, v142
	v_add_f32_e32 v158, v237, v141
	v_add_f32_e32 v142, v238, v142
	v_mfma_f32_32x32x16_bf16 v[96:111], a[216:219], a[184:187], v[96:111]
	ds_read_b64_tr_b16 v[66:67], v212 offset:0x3e00
	v_cvt_pk_bf16_f32 v141, v143, v243
	v_add_f32_e32 v143, v158, v143
	v_add_f32_e32 v158, v142, v243
	v_mfma_f32_32x32x16_bf16 v[48:63], a[248:251], a[152:155], v[48:63]
	s_mov_b32 s42, s17
	v_cvt_pk_bf16_f32 v142, v244, v245
	v_add_f32_e32 v159, v143, v244
	v_add_f32_e32 v158, v158, v245
	v_mfma_f32_32x32x16_bf16 v[32:47], a[248:251], a[184:187], v[32:47]
	s_add_i32 s43, s57, 0x80
	v_cvt_pk_bf16_f32 v143, v246, v247
	v_add_f32_e32 v159, v159, v246
	v_add_f32_e32 v158, v158, v247
	v_mfma_f32_32x32x16_bf16 v[112:127], a[220:223], a[156:159], v[112:127]
	s_mov_b32 s44, s18
	v_add_f32_e32 v159, v159, v148
	v_add_f32_e32 v158, v158, v149
	v_mfma_f32_32x32x16_bf16 v[96:111], a[220:223], a[188:191], v[96:111]
	v_add_f32_e32 v159, v159, v150
	v_add_f32_e32 v158, v158, v151
	v_mfma_f32_32x32x16_bf16 v[48:63], a[252:255], a[156:159], v[48:63]
	s_mov_b32 s45, s19
	v_add_f32_e32 v159, v159, v152
	v_add_f32_e32 v158, v158, v153
	v_mfma_f32_32x32x16_bf16 v[32:47], a[252:255], a[188:191], v[32:47]
	s_add_i32 s46, s57, 0x880
	v_add_f32_e32 v159, v159, v154
	v_add_f32_e32 v158, v158, v155
	v_add_f32_e32 v156, v156, v157
	s_waitcnt vmcnt(0) lgkmcnt(0)
	s_barrier
	s_mov_b32 m0, s0
	v_mfma_f32_32x32x16_bf16 a[0:15], v[180:183], v[168:171], a[0:15]
	buffer_load_dwordx4 v222, s[12:15], s1 offen lds
	v_mfma_f32_32x32x16_bf16 a[16:31], v[180:183], v[192:195], a[16:31]
	ds_read_b128 a[192:195], v218 offset:0
	s_mov_b32 m0, s35
	v_mfma_f32_32x32x16_bf16 a[32:47], v[184:187], v[168:171], a[32:47]
	buffer_load_dwordx4 v223, s[12:15], s36 offen lds
	v_add_f32_e32 v225, v225, v156
	v_add_f32_e32 v156, v159, v158
	ds_read_b128 a[196:199], v219 offset:0
	v_mfma_f32_32x32x16_bf16 a[48:63], v[184:187], v[192:195], a[48:63]
	ds_read_b128 a[200:203], v220 offset:0
	s_mov_b32 m0, s37
	v_mfma_f32_32x32x16_bf16 a[64:79], v[176:179], v[168:171], a[64:79]
	buffer_load_dwordx4 v222, s[12:15], s38 offen lds
	v_add_f32_e32 v226, v226, v156
	ds_read_b128 a[204:207], v221 offset:0
	v_mfma_f32_32x32x16_bf16 a[80:95], v[176:179], v[192:195], a[80:95]
	ds_read_b128 a[208:211], v218 offset:128
	s_mov_b32 m0, s39
	v_mfma_f32_32x32x16_bf16 a[96:111], v[188:191], v[168:171], a[96:111]
	buffer_load_dwordx4 v223, s[12:15], s40 offen lds
	ds_read_b128 a[212:215], v219 offset:128
	v_mfma_f32_32x32x16_bf16 a[112:127], v[188:191], v[192:195], a[112:127]
	ds_read_b128 a[216:219], v220 offset:128
	s_nop 0
	s_mov_b32 m0, s41
	v_mfma_f32_32x32x16_bf16 a[0:15], v[172:175], v[128:131], a[0:15]
	buffer_load_dwordx4 v196, s[4:7], s33 offen lds
	ds_read_b128 a[220:223], v221 offset:128
	s_cmp_gt_u32 s27, 12
	s_cbranch_scc1 .Lkc_done
	s_cmp_gt_u32 s27, 4
	s_cbranch_scc1 .Lkc_single
	v_cvt_pk_bf16_f32 v248, v248, v249
	v_cvt_pk_bf16_f32 v249, v250, v251
	v_cvt_pk_bf16_f32 v250, v252, v253
	v_cvt_pk_bf16_f32 v251, v254, v255
	v_lshrrev_b32_e32 v252, 1, v208
	buffer_store_dwordx4 v[248:251], v252, s[12:15], s56 offen sc1
	v_mbcnt_lo_u32_b32 v253, -1, 0
	v_mbcnt_hi_u32_b32 v253, -1, v253
	v_lshlrev_b32_e32 v253, 4, v253
	v_add_u32_e32 v253, s84, v253
	ds_read_b128 v[248:251], v253
	ds_read_b128 v[252:255], v253 offset:1024
	s_branch .Lkc_done

.Lkc_done:
	v_max3_f32 v156, v112, v113, v48
	v_max3_f32 v157, v114, v115, v49
	s_nop 0
	v_max3_f32 v156, v156, v50, v51
	v_mfma_f32_32x32x16_bf16 a[16:31], v[172:175], v[144:147], a[16:31]
	ds_read_b128 a[224:227], v218 offset:8192
	v_max3_f32 v156, v156, v116, v117
	v_max3_f32 v157, v157, v118, v119
	v_max3_f32 v156, v156, v52, v53
	v_max3_f32 v157, v157, v54, v55
	s_mov_b32 m0, s42
	v_mfma_f32_32x32x16_bf16 a[32:47], v[164:167], v[128:131], a[32:47]
	buffer_load_dwordx4 v196, s[4:7], s43 offen lds
	ds_read_b128 a[228:231], v219 offset:8192
	v_max3_f32 v156, v156, v120, v121
	v_max3_f32 v157, v157, v122, v123
	v_max3_f32 v156, v156, v56, v57
	v_max3_f32 v157, v157, v58, v59
	v_mfma_f32_32x32x16_bf16 a[48:63], v[164:167], v[144:147], a[48:63]
	ds_read_b128 a[232:235], v220 offset:8192
	v_max3_f32 v156, v156, v124, v125
	v_max3_f32 v157, v157, v126, v127
	v_max3_f32 v156, v156, v60, v61
	v_max3_f32 v157, v157, v62, v63
	s_mov_b32 m0, s44
	v_mfma_f32_32x32x16_bf16 a[64:79], v[160:163], v[128:131], a[64:79]
	buffer_load_dwordx4 v196, s[4:7], s34 offen lds
	ds_read_b128 a[236:239], v221 offset:8192
	v_max3_f32 v158, v96, v97, v32
	v_max3_f32 v159, v98, v99, v33
	v_max3_f32 v158, v158, v34, v35
	v_mfma_f32_32x32x16_bf16 a[80:95], v[160:163], v[144:147], a[80:95]
	ds_read_b128 a[240:243], v218 offset:8320
	v_max3_f32 v158, v158, v100, v101
	v_max3_f32 v159, v159, v102, v103
	v_max3_f32 v158, v158, v36, v37
	v_max3_f32 v159, v159, v38, v39
	s_mov_b32 m0, s45
	v_mfma_f32_32x32x16_bf16 a[96:111], v[136:139], v[128:131], a[96:111]
	buffer_load_dwordx4 v196, s[4:7], s46 offen lds
	ds_read_b128 a[244:247], v219 offset:8320
	v_max3_f32 v128, v158, v104, v105
	v_max3_f32 v129, v159, v106, v107
	v_max3_f32 v128, v128, v40, v41
	v_max3_f32 v129, v129, v42, v43
	v_mfma_f32_32x32x16_bf16 a[112:127], v[136:139], v[144:147], a[112:127]
	ds_read_b128 a[248:251], v220 offset:8320
	v_max3_f32 v128, v128, v108, v109
	v_max3_f32 v129, v129, v110, v111
	v_max3_f32 v128, v128, v44, v45
	v_max3_f32 v130, v129, v46, v47
	v_mfma_f32_32x32x16_bf16 a[0:15], v[132:135], v[84:87], a[0:15]
	ds_read_b128 a[252:255], v221 offset:8320
	s_cmp_gt_u32 s27, 4
	s_cbranch_scc1 .Lkd2_done
	s_waitcnt lgkmcnt(8)
	v_pk_add_f32 v[200:201], v[248:249], v[200:201]
	v_pk_add_f32 v[202:203], v[250:251], v[202:203]
	v_pk_add_f32 v[204:205], v[252:253], v[204:205]
	v_pk_add_f32 v[206:207], v[254:255], v[206:207]
	v_cvt_pk_bf16_f32 v248, v248, v249
	v_cvt_pk_bf16_f32 v249, v250, v251
	v_cvt_pk_bf16_f32 v250, v252, v253
	v_cvt_pk_bf16_f32 v251, v254, v255
	v_lshrrev_b32_e32 v252, 1, v208
	buffer_store_dwordx4 v[248:251], v252, s[4:7], s56 offen sc1
	s_add_i32 s56, s56, 0x1000
	s_nop 1
	global_load_dwordx4 v[248:251], v208, s[54:55] nt
	global_load_dwordx4 v[252:255], v208, s[54:55] offset:16 nt
	s_add_u32 s54, s54, 0x2000
	s_addc_u32 s55, s55, 0
	s_cmp_gt_u32 s27, 2
	s_cbranch_scc1 .Lkd2_done
	s_mov_b32 m0, s84
	s_nop 0
	buffer_load_dwordx4 v208, s[80:83], s86 offen lds
	s_mov_b32 m0, s85
	s_nop 0
	buffer_load_dwordx4 v208, s[80:83], s86 offen offset:16 lds
	s_add_i32 s86, s86, 0x2000
